# delay sort1 conversion blocks ~2.5us (s_sleep 85) so edge-list loads of the sort blocks get HBM first; plus hand layer2 + sc1 stores
# speedup vs baseline: 1.2813x; 1.0064x over previous
.LBB0_15:
	s_andn2_b64 vcc, exec, s[4:5]
	s_cbranch_vccnz .LBB0_21
	s_sleep 85
	s_load_dwordx2 s[10:11], s[0:1], 0x0
	s_load_dwordx2 s[8:9], s[0:1], 0x60
	s_lshl_b32 s3, s2, 1
	s_add_i32 s12, s3, 0xfffffe00
	s_mov_b32 s13, 0
	v_lshlrev_b32_e32 v4, 3, v0
	s_lshl_b64 s[4:5], s[12:13], 13
	v_or_b32_e32 v2, s4, v4
	v_mov_b32_e32 v3, s5
	s_waitcnt lgkmcnt(0)
	v_lshl_add_u64 v[6:7], v[2:3], 2, s[10:11]
	global_load_dwordx4 v[12:15], v[6:7], off
	global_load_dwordx4 v[16:19], v[6:7], off offset:16
	v_mbcnt_lo_u32_b32 v1, -1, 0
	v_mbcnt_hi_u32_b32 v1, -1, v1
	v_and_b32_e32 v6, 64, v1
	v_xor_b32_e32 v5, 1, v1
	v_add_u32_e32 v9, 64, v6
	v_cmp_lt_i32_e32 vcc, v5, v9
	v_xor_b32_e32 v7, 2, v1
	v_xor_b32_e32 v20, 8, v1
	v_cndmask_b32_e32 v5, v1, v5, vcc
	v_lshlrev_b32_e32 v6, 2, v5
	v_cmp_lt_i32_e32 vcc, v7, v9
	v_and_b32_e32 v10, 15, v0
	v_cmp_eq_u32_e64 s[4:5], 0, v10
	v_cndmask_b32_e32 v7, v1, v7, vcc
	v_lshlrev_b32_e32 v7, 2, v7
	s_mov_b32 s3, 0x42fe0000
	s_waitcnt vmcnt(1)
	v_max3_f32 v5, |v12|, 0, |v13|
	v_max3_f32 v5, v5, |v14|, |v15|
	s_waitcnt vmcnt(0)
	v_max3_f32 v5, v5, |v16|, |v17|
	v_max3_f32 v5, v5, |v18|, |v19|
	ds_bpermute_b32 v8, v6, v5
	s_waitcnt lgkmcnt(0)
	v_max_f32_e32 v8, v8, v8
	v_max_f32_e32 v5, v5, v8
	ds_bpermute_b32 v11, v7, v5
	v_xor_b32_e32 v8, 4, v1
	v_cmp_lt_i32_e32 vcc, v8, v9
	s_waitcnt lgkmcnt(0)
	v_max_f32_e32 v11, v11, v11
	v_cndmask_b32_e32 v8, v1, v8, vcc
	v_lshlrev_b32_e32 v8, 2, v8
	v_max_f32_e32 v5, v5, v11
	ds_bpermute_b32 v11, v8, v5
	v_cmp_lt_i32_e32 vcc, v20, v9
	s_nop 1
	v_cndmask_b32_e32 v1, v1, v20, vcc
	v_lshlrev_b32_e32 v9, 2, v1
	s_waitcnt lgkmcnt(0)
	v_max_f32_e32 v1, v11, v11
	v_max_f32_e32 v11, v5, v1
	ds_bpermute_b32 v20, v9, v11
	v_mov_b32_e32 v1, 0x8000
	v_mov_b32_e32 v5, 0x800000
	s_waitcnt lgkmcnt(0)
	v_max_f32_e32 v10, v20, v20
	v_max_f32_e32 v10, v11, v10
	v_div_scale_f32 v11, s[14:15], v10, v10, s3
	v_rcp_f32_e32 v22, v11
	v_div_scale_f32 v23, vcc, s3, v10, s3
	v_lshl_add_u64 v[20:21], s[8:9], 0, v[2:3]
	v_fma_f32 v24, -v11, v22, 1.0
	v_fmac_f32_e32 v22, v24, v22
	v_mul_f32_e32 v24, v23, v22
	v_fma_f32 v25, -v11, v24, v23
	v_fmac_f32_e32 v24, v25, v22
	v_fma_f32 v11, -v11, v24, v23
	v_div_fmas_f32 v11, v11, v22, v24
	v_div_fixup_f32 v11, v11, v10, s3
	v_cmp_lt_f32_e32 vcc, 0, v10
	s_nop 1
	v_cndmask_b32_e32 v11, 0, v11, vcc
	v_mul_f32_e32 v12, v12, v11
	v_mul_f32_e32 v16, v16, v11
	v_mul_f32_e32 v13, v13, v11
	v_mul_f32_e32 v17, v17, v11
	v_mul_f32_e32 v14, v14, v11
	v_mul_f32_e32 v18, v18, v11
	v_rndne_f32_e32 v12, v12
	v_rndne_f32_e32 v16, v16
	v_rndne_f32_e32 v13, v13
	v_rndne_f32_e32 v17, v17
	v_mul_f32_e32 v15, v15, v11
	v_mul_f32_e32 v11, v19, v11
	v_rndne_f32_e32 v14, v14
	v_rndne_f32_e32 v18, v18
	v_cvt_i32_f32_e32 v12, v12
	v_cvt_i32_f32_e32 v16, v16
	v_cvt_i32_f32_e32 v13, v13
	v_cvt_i32_f32_e32 v17, v17
	v_rndne_f32_e32 v15, v15
	v_rndne_f32_e32 v11, v11
	v_cvt_i32_f32_e32 v14, v14
	v_cvt_i32_f32_e32 v18, v18
	v_cvt_i32_f32_sdwa v15, v15 dst_sel:BYTE_3 dst_unused:UNUSED_PAD src0_sel:DWORD
	v_cvt_i32_f32_sdwa v11, v11 dst_sel:BYTE_3 dst_unused:UNUSED_PAD src0_sel:DWORD
	v_add_u32_e32 v16, 0x80, v16
	v_add_u32_e32 v12, 0x80, v12
	v_lshl_add_u32 v17, v17, 8, v1
	v_lshl_add_u32 v13, v13, 8, v1
	v_lshl_add_u32 v18, v18, 16, v5
	v_lshl_add_u32 v14, v14, 16, v5
	v_or_b32_e32 v16, v17, v16
	v_or_b32_e32 v12, v13, v12
	v_xor_b32_e32 v11, 0x80000000, v11
	v_xor_b32_e32 v15, 0x80000000, v15
	v_or_b32_e32 v13, v16, v18
	v_or_b32_e32 v12, v12, v14
	v_or_b32_e32 v13, v13, v11
	v_or_b32_e32 v12, v12, v15
	global_store_dwordx2 v[20:21], v[12:13], off
	s_and_saveexec_b64 s[14:15], s[4:5]
	s_cbranch_execz .LBB0_18
	s_mov_b32 s16, 0x3c010204
	v_lshrrev_b64 v[2:3], 6, v[2:3]
	v_fma_mixlo_f16 v10, v10, s16, 0
	v_lshl_add_u64 v[2:3], s[6:7], 0, v[2:3]
	global_store_short v[2:3], v10, off
